# static priority raise for the compute waves (0-3) during light-tile K-loops; staging waves keep priority 0
# baseline (speedup 1.0000x reference)
; #define G_DMA_A(buf, t, i_) __builtin_amdgcn_raw_ptr_buffer_load_lds(ra, (LAS void*)(lds + (buf) * 65536 + a_wu + (i_) * 8192), 16, ao##i_, (unsigned)(t) * 128u, 0, 0)
; #define G_ISSUE_B(t) do { const unsigned so_ = (unsigned)(t) * 64u * ldbB; _Pragma("unroll") for (int i_ = 0; i_ < 8; ++i_) sb[i_] = __builtin_bit_cast(f32x4, __builtin_amdgcn_raw_buffer_load_b128(rb, bo, so_ + (unsigned)i_ * ldbB, 0)); } while (0)
; #define G_RETIRE() asm volatile("s_waitcnt vmcnt(0)" : "+v"(sb[0]), "+v"(sb[1]), "+v"(sb[2]), "+v"(sb[3]), "+v"(sb[4]), "+v"(sb[5]), "+v"(sb[6]), "+v"(sb[7]) :: "memory")
; __device__ __forceinline__ void gemm_kloop_light(f32x4 (&acc)[8][4], LAS unsigned char* lds, const GemmT& T, ...
;     ...
;     G_ISSUE_B(0); G_DMA_A(0, 0, 0); G_DMA_A(0, 0, 1); G_DMA_A(0, 0, 2); G_DMA_A(0, 0, 3); G_RETIRE(); G_WRITE_B(0);
;     if (nt > 1) G_ISSUE_B(1);
;     G_BAR();
;     for (int t = 0; t < nt; ++t) { const int cur = t & 1; const bool w1 = t + 1 < nt, i2 = t + 2 < nt;
;         if (w1) { G_DMA_A(cur ^ 1, t + 1, 0); G_DMA_A(cur ^ 1, t + 1, 1); G_DMA_A(cur ^ 1, t + 1, 2); G_DMA_A(cur ^ 1, t + 1, 3); }
;         if (mlim > 0) {
; __device__ __forceinline__ void phase_moe_gu(const Ptrs& p, LAS unsigned char* lds) {
;     ...
;     for (int u = vwg_id(); moe_unit(cv, u, 16, mu); u += gridDim.x) {
;         GemmT T; T.init();
;         const int* list = (const int*)(p.ws + OFF_LIST) + (size_t)mu.e * NTOK; const int i0 = mu.mt * 256, n0 = mu.nt * 128;
;         unsigned ao[4];
; #pragma unroll
;         for (int i = 0; i < 4; ++i) { const int r = i0 + T.aR + 64 * i; const int tok = (r < mu.cnt) ? (list[r] >> 2) : 0; ao[i] = (unsigned)((tok * D + T.aC) * 2); }
;         const float* wsel = ((__builtin_amdgcn_readfirstlane(T.b_p) & 1) ? p.w_up : p.w_gate) + (size_t)mu.e * D * D + n0;
;         const unsigned bo = (unsigned)((T.b_k * D + T.b_gucol) * 4);
;         f32x4 acc[8][4]; acc_zero(acc);
;         const int mlim = __builtin_amdgcn_readfirstlane(T.wr) ? 0 : ((mu.cnt - i0 + 15) >> 4);
;         if (mu.light) gemm_kloop_light(acc, lds, T, mk_rsrc(h2), ao[0], ao[1], ao[2], ao[3], mk_rsrc(wsel), bo, D * 4u, D / 64, mlim);
;         else gemm_kloop(acc, lds, T, mk_rsrc(h2), ao[0], ao[1], ao[2], ao[3], mk_rsrc(wsel), bo, D * 4u, D / 64);
.LBB0_1163:
	s_andn2_b64 vcc, exec, s[0:1]
	s_mov_b64 s[0:1], -1
	s_cbranch_vccnz .LBB0_1005
	s_ashr_i32 s43, s42, 31
	s_lshl_b64 s[0:1], s[42:43], 15
	v_mov_b32_e32 v3, v0
	s_add_u32 s0, s52, s0
	s_addc_u32 s1, s53, s1
	v_bfe_u32 v4, v3, 2, 4
	s_lshl_b32 s2, s86, 8
	v_ashrrev_i32_e32 v10, 7, v3
	v_or_b32_e32 v4, s2, v4
	v_lshl_add_u32 v4, v10, 4, v4
	v_cmp_gt_i32_e32 vcc, s87, v4
	v_mov_b32_e32 v6, 0
	v_ashrrev_i32_e32 v5, 31, v4
	v_mov_b32_e32 v7, 0
	v_mov_b32_e32 v8, 0
	v_mov_b32_e32 v9, 0
	v_lshl_add_u64 v[12:13], v[4:5], 2, s[0:1]
	s_and_saveexec_b64 s[4:5], vcc
	global_load_dword v7, v[12:13], off
	s_or_b64 exec, exec, s[4:5]
	v_add_u32_e32 v11, 64, v4
	v_cmp_gt_i32_e32 vcc, s87, v11
	s_and_saveexec_b64 s[4:5], vcc
	global_load_dword v6, v[12:13], off offset:256
	s_or_b64 exec, exec, s[4:5]
	v_add_u32_e32 v11, 0x80, v4
	v_cmp_gt_i32_e32 vcc, s87, v11
	s_and_saveexec_b64 s[4:5], vcc
	global_load_dword v9, v[12:13], off offset:512
	s_or_b64 exec, exec, s[4:5]
	v_add_u32_e32 v11, 0xc0, v4
	v_cmp_gt_i32_e32 vcc, s87, v11
	s_and_saveexec_b64 s[4:5], vcc
	global_load_dword v8, v[12:13], off offset:768
	s_or_b64 exec, exec, s[4:5]
	v_ashrrev_i32_e32 v5, 6, v3
	v_and_b32_e32 v11, 1, v5
	s_lshl_b32 s0, s85, 7
	v_readfirstlane_b32 s1, v11
	v_readlane_b32 s4, v246, 0
	s_bitcmp0_b32 s1, 0
	v_readlane_b32 s5, v246, 1
	s_cselect_b32 s1, s49, s5
	s_cselect_b32 s3, s48, s4
	s_lshl_b64 s[4:5], s[42:43], 24
	v_readlane_b32 s6, v246, 2
	s_add_u32 s3, s3, s4
	v_and_b32_e32 v4, 63, v3
	s_addc_u32 s6, s1, s5
	s_ashr_i32 s1, s0, 31
	v_lshrrev_b32_e32 v12, 5, v4
	v_bfe_u32 v13, v3, 1, 2
	s_lshl_b64 s[4:5], s[0:1], 2
	v_lshl_or_b32 v10, v10, 1, v12
	v_bfe_u32 v12, v3, 3, 2
	v_and_b32_e32 v14, 1, v3
	v_lshlrev_b32_e32 v15, 5, v13
	s_add_u32 s24, s3, s4
	v_lshl_or_b32 v15, v12, 7, v15
	v_lshlrev_b32_e32 v16, 16, v10
	v_lshlrev_b32_e32 v17, 4, v14
	s_addc_u32 s1, s6, s5
	v_or3_b32 v225, v15, v17, v16
	s_and_b32 s25, s1, 0xffff
	s_movk_i32 s1, 0x2000
	buffer_load_dwordx4 v[114:117], v225, s[24:27], 0 offen
	buffer_load_dwordx4 v[118:121], v225, s[24:27], s66 offen
	s_mov_b32 s3, 0x8000
	buffer_load_dwordx4 v[126:129], v225, s[24:27], s1 offen
	buffer_load_dwordx4 v[122:125], v225, s[24:27], s3 offen
	s_movk_i32 s1, 0x4000
	s_mov_b32 s3, 0xa000
	buffer_load_dwordx4 v[130:133], v225, s[24:27], s1 offen
	buffer_load_dwordx4 v[134:137], v225, s[24:27], s3 offen
	s_mov_b32 s1, 0xc000
	s_mov_b32 s3, 0xe000
	buffer_load_dwordx4 v[142:145], v225, s[24:27], s1 offen
	buffer_load_dwordx4 v[146:149], v225, s[24:27], s3 offen
	s_waitcnt vmcnt(8)
	v_lshlrev_b32_e32 v7, 10, v7
	v_and_b32_e32 v7, 0xfffff000, v7
	v_lshlrev_b32_e32 v6, 10, v6
	v_and_b32_e32 v6, 0xfffff000, v6
	v_lshlrev_b32_e32 v9, 10, v9
	v_and_b32_e32 v9, 0xfffff000, v9
	v_lshlrev_b32_e32 v8, 10, v8
	v_and_b32_e32 v8, 0xfffff000, v8
	v_lshlrev_b32_e32 v17, 4, v3
	v_lshlrev_b32_e32 v15, 6, v11
	v_and_b32_e32 v16, 32, v3
	v_and_b32_e32 v17, 48, v17
	v_bitop3_b32 v15, v17, v15, v16 bitop3:0xde
	v_or_b32_e32 v221, v9, v15
	v_lshlrev_b32_e32 v9, 2, v12
	v_lshlrev_b32_e32 v11, 1, v11
	v_or3_b32 v9, v9, v11, v14
	v_lshlrev_b32_e32 v11, 2, v3
	v_and_b32_e32 v12, 0xfffffc00, v11
	v_lshl_add_u32 v9, v9, 11, v12
	v_lshlrev_b32_e32 v12, 8, v13
	v_lshlrev_b32_e32 v10, 4, v10
	v_and_or_b32 v10, v10, 48, v12
	v_lshlrev_b32_e32 v12, 3, v3
	v_or_b32_e32 v223, v7, v15
	v_and_b32_e32 v7, 15, v3
	v_and_b32_e32 v12, 32, v12
	v_or_b32_e32 v222, v6, v15
	v_ashrrev_i32_e32 v6, 8, v3
	v_bitop3_b32 v219, v9, v10, v12 bitop3:0xf6
	v_lshlrev_b32_e32 v7, 6, v7
	v_and_b32_e32 v3, 48, v3
	v_and_b32_e32 v10, 32, v11
	v_or_b32_e32 v9, v7, v3
	v_bitop3_b32 v3, v7, v10, v3 bitop3:0x36
	v_lshlrev_b32_e32 v11, 13, v5
	v_lshlrev_b32_e32 v220, 6, v14
	v_lshlrev_b32_e32 v4, 4, v4
	v_lshlrev_b32_e32 v7, 14, v6
	v_and_or_b32 v226, v11, s66, v3
	v_cmp_eq_u32_e32 vcc, 0, v215
	v_add_u32_e32 v227, 0, v219
	v_add_u32_e32 v3, 0xc0, v220
	v_or_b32_e32 v224, v8, v15
	v_lshl_or_b32 v229, v5, 10, v4
	v_bitop3_b32 v216, v9, v7, v10 bitop3:0xde
	v_or_b32_e32 v217, 0x8000, v226
	v_readfirstlane_b32 s1, v6
	s_and_b64 vcc, exec, vcc
	v_add_u32_e32 v228, v227, v220
	v_and_b32_e32 v218, 0xc0, v3
	v_readlane_b32 s7, v246, 3
	v_readlane_b32 s8, v246, 4
	v_readlane_b32 s9, v246, 5
	v_readlane_b32 s10, v246, 6
	v_readlane_b32 s11, v246, 7
	s_cbranch_vccnz .LBB0_1263
	s_sub_i32 s3, s87, s2
	s_mov_b32 s99, s3
	v_readfirstlane_b32 s100, v0
	s_nop 3
	s_lshr_b32 s100, s100, 7
	s_lshl_b32 s100, s100, 4
	s_add_i32 s3, s3, 15
	s_cmp_ge_i32 s100, 32
	s_cbranch_scc1 .Lmy_lp0
	s_setprio 1
.Lmy_lp0:
	s_ashr_i32 s3, s3, 4
	s_cmp_eq_u32 s1, 0
	s_cselect_b32 s1, s3, 0
	v_readfirstlane_b32 s3, v229
	s_and_b32 s3, s3, 0xfffffc00
	s_add_i32 s3, s3, 0
	s_mov_b32 s38, s26
	s_mov_b32 s39, s27
	s_mov_b32 m0, s3
	s_waitcnt vmcnt(6)
	v_mov_b64_e32 v[4:5], v[118:119]
	buffer_load_dwordx4 v223, s[36:39], 0 offen lds
	s_add_i32 m0, s3, 0x2000
	s_waitcnt vmcnt(3)
	v_mov_b64_e32 v[8:9], v[134:135]
	buffer_load_dwordx4 v222, s[36:39], 0 offen lds
	s_add_i32 m0, s3, 0x4000
	v_mov_b64_e32 v[12:13], v[114:115]
	buffer_load_dwordx4 v221, s[36:39], 0 offen lds
	s_add_i32 m0, s3, 0x6000
	s_waitcnt vmcnt(3)
	v_mov_b64_e32 v[16:17], v[146:147]
	v_mov_b64_e32 v[20:21], v[130:131]
	v_mov_b64_e32 v[24:25], v[122:123]
	v_mov_b64_e32 v[28:29], v[142:143]
	v_mov_b64_e32 v[32:33], v[126:127]
	buffer_load_dwordx4 v224, s[36:39], 0 offen lds
	v_mov_b64_e32 v[6:7], v[120:121]
	v_mov_b64_e32 v[10:11], v[136:137]
	v_mov_b64_e32 v[14:15], v[116:117]
	v_mov_b64_e32 v[18:19], v[148:149]
	v_mov_b64_e32 v[22:23], v[132:133]
	v_mov_b64_e32 v[26:27], v[124:125]
	v_mov_b64_e32 v[30:31], v[144:145]
	v_mov_b64_e32 v[34:35], v[128:129]
	s_waitcnt vmcnt(0)
	s_movk_i32 s101, 0x80
	s_cmp_le_i32 s99, s100
	s_cbranch_scc1 .Lmy_rcgP0
	buffer_load_dwordx4 v[236:239], v223, s[36:39], s101 offen

; #define LAS __attribute__((address_space(3)))
; #define G_DMA_A(buf, t, i_) __builtin_amdgcn_raw_ptr_buffer_load_lds(ra, (LAS void*)(lds + (buf) * 65536 + a_wu + (i_) * 8192), 16, ao##i_, (unsigned)(t) * 128u, 0, 0)
; #define G_ISSUE_B(t) do { const unsigned so_ = (unsigned)(t) * 64u * ldbB; _Pragma("unroll") for (int i_ = 0; i_ < 8; ++i_) sb[i_] = __builtin_bit_cast(f32x4, __builtin_amdgcn_raw_buffer_load_b128(rb, bo, so_ + (unsigned)i_ * ldbB, 0)); } while (0)
; #define G_RETIRE() asm volatile("s_waitcnt vmcnt(0)" : "+v"(sb[0]), "+v"(sb[1]), "+v"(sb[2]), "+v"(sb[3]), "+v"(sb[4]), "+v"(sb[5]), "+v"(sb[6]), "+v"(sb[7]) :: "memory")
; #define G_WRITE_B(buf) do { LAS unsigned char* d_ = lds + (buf) * 65536; \
;         _Pragma("unroll") for (int j_ = 0; j_ < 4; ++j_) { u32x4 w_; w_.x = cvtpk(sb[0][j_], sb[1][j_]); w_.y = cvtpk(sb[2][j_], sb[3][j_]); w_.z = cvtpk(sb[4][j_], sb[5][j_]); w_.w = cvtpk(sb[6][j_], sb[7][j_]); \
;             *(LAS u32x4*)(d_ + 32768 + T.b_w + ((T.b_rot + 64u * j_) & 255u)) = w_; } } while (0)
; #define G_BAR() do { asm volatile("s_waitcnt lgkmcnt(0)" ::: "memory"); __builtin_amdgcn_s_barrier(); asm volatile("" ::: "memory"); } while (0)
; __device__ __forceinline__ void gemm_kloop_light(f32x4 (&acc)[8][4], LAS unsigned char* lds, const GemmT& T, ...
;     ...
;     for (int t = 0; t < nt; ++t) { const int cur = t & 1; const bool w1 = t + 1 < nt, i2 = t + 2 < nt;
;         if (w1) { G_DMA_A(cur ^ 1, t + 1, 0); G_DMA_A(cur ^ 1, t + 1, 1); G_DMA_A(cur ^ 1, t + 1, 2); G_DMA_A(cur ^ 1, t + 1, 3); }
;         if (mlim > 0) {
; #pragma unroll
;             for (int ks = 0; ks < 2; ++ks) { const LAS unsigned char* s_ = lds + cur * 65536 + ks * 1024; bf16x8 Bf_[4];
; #pragma unroll
;                 for (int n_ = 0; n_ < 4; ++n_) Bf_[n_] = *(const LAS bf16x8*)(s_ + T.b_r + n_ * 2048);
; #pragma unroll
;                 for (int m_ = 0; m_ < 8; ++m_) if (m_ < mlim) { const bf16x8 At_ = *(const LAS bf16x8*)(s_ + T.a_r + m_ * 2048);
; #pragma unroll
;                     for (int n_ = 0; n_ < 4; ++n_) acc[m_][n_] = __builtin_amdgcn_mfma_f32_16x16x32_bf16(Bf_[n_], At_, acc[m_][n_], 0, 0, 0); } } }
;         if (w1) { G_RETIRE(); G_WRITE_B(cur ^ 1); }
;         if (i2) G_ISSUE_B(t + 2);
;         G_BAR(); }
.LBB0_1238:
	s_setprio 0
	s_waitcnt lgkmcnt(0)
	s_barrier
	s_branch .LBB0_1267

; __device__ __forceinline__ int tid_opaque() { int t = threadIdx.x; asm volatile("" : "+v"(t)); return t; }
; __device__ __forceinline__ __amdgpu_buffer_rsrc_t mk_rsrc(const void* p) { return __builtin_amdgcn_make_buffer_rsrc((void*)p, 0, 0x7ffffff0, 0x00020000); }
; __device__ __forceinline__ void phase_moe_down(const Ptrs& p, LAS unsigned char* lds) {
;     ...
;         GemmT T; T.init();
;         const int* list = (const int*)(p.ws + OFF_LIST) + (size_t)mu.e * NTOK; const int i0 = mu.mt * 256, col0 = mu.nt * 256;
;         const unsigned ao = (unsigned)((T.aR * D + T.aC) * 2), bo = (unsigned)((T.b_k * D + T.b_col) * 4);
;         int pa = -1; float pg = 0.f;
;         { const int t_ = tid_opaque(); if (t_ < 256 && i0 + t_ < mu.cnt) { pa = list[i0 + t_]; pg = gate[pa]; } }
;         f32x4 acc[8][4]; acc_zero(acc);
;         const int mlim = __builtin_amdgcn_readfirstlane(T.wr) ? 0 : ((mu.cnt - i0 + 15) >> 4);
;         if (mu.light) gemm_kloop_light(acc, lds, T, mk_rsrc(act + (size_t)(mu.base + i0) * D), ao, ao + 64u * 4096, ao + 128u * 4096, ao + 192u * 4096,
;                                        mk_rsrc(p.w_down + (size_t)mu.e * D * D + col0), bo, D * 4u, D / 64, mlim);
;         else gemm_kloop(acc, lds, T, mk_rsrc(act + (size_t)(mu.base + i0) * D), ao, ao + 64u * 4096, ao + 128u * 4096, ao + 192u * 4096,
;                         mk_rsrc(p.w_down + (size_t)mu.e * D * D + col0), bo, D * 4u, D / 64);
.LBB0_1483:
	s_or_b64 exec, exec, s[0:1]
	s_add_i32 s2, s84, s85
	s_ashr_i32 s3, s2, 31
	s_lshl_b32 s0, s81, 8
	s_lshl_b64 s[2:3], s[2:3], 12
	s_add_u32 s36, s20, s2
	v_readlane_b32 s4, v246, 0
	s_addc_u32 s1, s28, s3
	v_readlane_b32 s5, v246, 1
	v_readlane_b32 s6, v246, 2
	v_readlane_b32 s7, v246, 3
	v_readlane_b32 s8, v246, 4
	v_readlane_b32 s9, v246, 5
	s_and_b32 s37, s1, 0xffff
	s_lshl_b64 s[2:3], s[42:43], 24
	v_readlane_b32 s10, v246, 6
	v_readlane_b32 s11, v246, 7
	s_mov_b64 s[4:5], s[8:9]
	s_add_u32 s4, s4, s2
	v_ashrrev_i32_e32 v4, 6, v3
	v_bfe_u32 v11, v3, 1, 2
	s_addc_u32 s5, s5, s3
	s_ashr_i32 s1, s0, 31
	v_ashrrev_i32_e32 v5, 7, v3
	v_and_b32_e32 v6, 1, v4
	v_bfe_u32 v8, v3, 5, 1
	v_bfe_u32 v10, v3, 3, 2
	v_and_b32_e32 v12, 1, v3
	v_lshlrev_b32_e32 v14, 3, v11
	s_lshl_b64 s[2:3], s[0:1], 2
	v_lshlrev_b32_e32 v7, 5, v6
	v_lshl_or_b32 v9, v5, 1, v8
	v_lshl_or_b32 v14, v10, 6, v14
	v_lshlrev_b32_e32 v15, 2, v12
	s_add_u32 s24, s4, s2
	v_lshlrev_b32_e32 v13, 16, v9
	v_or3_b32 v14, v14, v15, v7
	s_addc_u32 s1, s5, s3
	v_lshl_or_b32 v222, v14, 2, v13
	s_and_b32 s25, s1, 0xffff
	s_movk_i32 s1, 0x2000
	buffer_load_dwordx4 v[110:113], v222, s[24:27], 0 offen
	buffer_load_dwordx4 v[114:117], v222, s[24:27], s66 offen
	s_mov_b32 s2, 0x8000
	buffer_load_dwordx4 v[122:125], v222, s[24:27], s1 offen
	buffer_load_dwordx4 v[118:121], v222, s[24:27], s2 offen
	s_movk_i32 s1, 0x4000
	s_mov_b32 s2, 0xa000
	buffer_load_dwordx4 v[126:129], v222, s[24:27], s1 offen
	buffer_load_dwordx4 v[130:133], v222, s[24:27], s2 offen
	s_mov_b32 s1, 0xc000
	s_mov_b32 s2, 0xe000
	buffer_load_dwordx4 v[138:141], v222, s[24:27], s1 offen
	buffer_load_dwordx4 v[142:145], v222, s[24:27], s2 offen
	s_waitcnt vmcnt(8)
	v_cmp_ne_u32_e32 vcc, -1, v214
	s_and_saveexec_b64 vcc, vcc
	v_ashrrev_i32_e32 v17, 31, v214
	v_mov_b32_e32 v16, v214
	v_lshl_add_u64 v[16:17], v[16:17], 2, s[56:57]
	global_load_dword v215, v[16:17], off
	s_or_b64 exec, exec, vcc
	v_lshlrev_b32_e32 v16, 3, v3
	v_and_b32_e32 v13, 63, v3
	v_lshlrev_b32_e32 v8, 4, v8
	v_and_b32_e32 v17, 24, v16
	v_bitop3_b32 v7, v8, v7, v17 bitop3:0xde
	v_lshlrev_b32_e32 v8, 4, v13
	v_lshl_or_b32 v230, v4, 10, v8
	v_lshlrev_b32_e32 v8, 2, v10
	v_lshlrev_b32_e32 v6, 1, v6
	v_or3_b32 v6, v8, v6, v12
	v_lshlrev_b32_e32 v8, 2, v3
	v_and_b32_e32 v10, 0xfffffc00, v8
	v_lshl_add_u32 v6, v6, 11, v10
	v_lshlrev_b32_e32 v10, 8, v11
	v_lshlrev_b32_e32 v9, 4, v9
	v_and_b32_e32 v15, 15, v3
	v_and_or_b32 v9, v9, 48, v10
	v_and_b32_e32 v10, 32, v16
	v_bitop3_b32 v220, v6, v9, v10 bitop3:0xf6
	v_lshlrev_b32_e32 v6, 6, v15
	v_and_b32_e32 v9, 48, v3
	v_and_b32_e32 v8, 32, v8
	v_or_b32_e32 v10, v6, v9
	v_bitop3_b32 v6, v6, v8, v9 bitop3:0x36
	v_lshlrev_b32_e32 v4, 13, v4
	v_ashrrev_i32_e32 v14, 8, v3
	v_and_or_b32 v227, v4, s66, v6
	v_lshlrev_b32_e32 v4, 16, v5
	v_lshlrev_b32_e32 v3, 10, v3
	s_mov_b32 s1, 0xf000
	v_lshlrev_b32_e32 v219, 6, v12
	v_and_or_b32 v3, v3, s1, v4
	v_lshlrev_b32_e32 v9, 14, v14
	v_lshl_or_b32 v225, v7, 1, v3
	v_cmp_eq_u32_e32 vcc, 0, v216
	v_add_u32_e32 v228, 0, v220
	v_add_u32_e32 v3, 0xc0, v219
	v_bitop3_b32 v217, v10, v9, v8 bitop3:0xde
	v_or_b32_e32 v218, 0x8000, v227
	v_readfirstlane_b32 s1, v14
	v_add_u32_e32 v226, 0x40000, v225
	v_add_u32_e32 v224, 0x80000, v225
	v_add_u32_e32 v223, 0xc0000, v225
	v_add_u32_e32 v229, v228, v219
	v_and_b32_e32 v221, 0xc0, v3
	s_mov_b64 s[6:7], s[10:11]
	s_cbranch_vccnz .LBB0_1574
	s_sub_i32 s2, s83, s85
	s_mov_b32 s99, s2
	v_readfirstlane_b32 s100, v0
	s_nop 3
	s_lshr_b32 s100, s100, 7
	s_lshl_b32 s100, s100, 4
	s_add_i32 s2, s2, 15
	s_cmp_ge_i32 s100, 32
	s_cbranch_scc1 .Lmy_lp1
	s_setprio 1
.Lmy_lp1:
	s_ashr_i32 s2, s2, 4
	s_cmp_eq_u32 s1, 0
	s_cselect_b32 s1, s2, 0
	v_readfirstlane_b32 s2, v230
	s_and_b32 s2, s2, 0xfffffc00
	s_add_i32 s2, s2, 0
	s_mov_b32 s38, s26
	s_mov_b32 s39, s27
	s_mov_b32 m0, s2
	s_waitcnt vmcnt(4)
	v_mov_b64_e32 v[4:5], v[118:119]
	buffer_load_dwordx4 v225, s[36:39], 0 offen lds
	s_add_i32 m0, s2, 0x2000
	s_waitcnt vmcnt(2)
	v_mov_b64_e32 v[8:9], v[138:139]
	buffer_load_dwordx4 v226, s[36:39], 0 offen lds
	s_add_i32 m0, s2, 0x4000
	v_mov_b64_e32 v[12:13], v[122:123]
	buffer_load_dwordx4 v224, s[36:39], 0 offen lds
	s_add_i32 m0, s2, 0x6000
	v_mov_b64_e32 v[16:17], v[114:115]
	v_mov_b64_e32 v[20:21], v[130:131]
	v_mov_b64_e32 v[24:25], v[110:111]
	s_waitcnt vmcnt(3)
	v_mov_b64_e32 v[28:29], v[142:143]
	v_mov_b64_e32 v[32:33], v[126:127]
	buffer_load_dwordx4 v223, s[36:39], 0 offen lds
	v_mov_b64_e32 v[6:7], v[120:121]
	v_mov_b64_e32 v[10:11], v[140:141]
	v_mov_b64_e32 v[14:15], v[124:125]
	v_mov_b64_e32 v[18:19], v[116:117]
	v_mov_b64_e32 v[22:23], v[132:133]
	v_mov_b64_e32 v[26:27], v[112:113]
	v_mov_b64_e32 v[30:31], v[144:145]
	v_mov_b64_e32 v[34:35], v[128:129]
	s_waitcnt vmcnt(0)
	s_movk_i32 s101, 0x80
	s_cmp_le_i32 s99, s100
	s_cbranch_scc1 .Lmy_rcdP0
	buffer_load_dwordx4 v[236:239], v225, s[36:39], s101 offen
